# baseline (speedup 1.0000x reference)
.LBB0_6:
	s_load_dwordx4 s[12:15], s[0:1], 0x10
	s_load_dwordx2 s[16:17], s[0:1], 0x20
	v_and_b32_e32 v33, 15, v0
	v_bfe_u32 v32, v0, 4, 2
	v_mov_b32_e32 v1, 0
	v_accvgpr_write_b32 a0, 0
	v_accvgpr_write_b32 a1, 0
	v_accvgpr_write_b32 a2, 0
	v_accvgpr_write_b32 a3, 0
	v_accvgpr_write_b32 a4, 0
	v_accvgpr_write_b32 a5, 0
	v_accvgpr_write_b32 a6, 0
	v_accvgpr_write_b32 a7, 0
	v_accvgpr_write_b32 a8, 0
	v_accvgpr_write_b32 a9, 0
	v_accvgpr_write_b32 a10, 0
	v_accvgpr_write_b32 a11, 0
	v_accvgpr_write_b32 a12, 0
	v_accvgpr_write_b32 a13, 0
	v_accvgpr_write_b32 a14, 0
	s_andn2_b64 vcc, exec, s[18:19]
	v_accvgpr_write_b32 a15, 0
	s_cbranch_vccnz .LBB0_16
	v_lshrrev_b32_e32 v44, 4, v0
	v_and_b32_e32 v36, 0x78, v4
	v_or_b32_e32 v4, s20, v44
	v_min_i32_e32 v0, s25, v4
	v_mad_i64_i32 v[2:3], s[0:1], v0, s10, 0
	v_or_b32_e32 v5, s22, v44
	s_waitcnt lgkmcnt(0)
	v_lshl_add_u64 v[2:3], v[2:3], 1, s[4:5]
	v_lshlrev_b32_e32 v0, 1, v36
	v_lshl_add_u64 v[16:17], v[2:3], 0, v[0:1]
	v_min_i32_e32 v2, s24, v5
	v_mad_i64_i32 v[2:3], s[0:1], v2, s10, 0
	v_lshl_add_u64 v[2:3], v[2:3], 1, s[6:7]
	v_lshl_add_u64 v[18:19], v[2:3], 0, v[0:1]
	v_add_u32_e32 v2, 16, v4
	v_min_i32_e32 v2, s25, v2
	v_mad_i64_i32 v[2:3], s[0:1], v2, s10, 0
	v_lshl_add_u64 v[2:3], v[2:3], 1, s[4:5]
	v_lshl_add_u64 v[20:21], v[2:3], 0, v[0:1]
	v_add_u32_e32 v2, 16, v5
	v_min_i32_e32 v2, s24, v2
	v_mad_i64_i32 v[2:3], s[0:1], v2, s10, 0
	v_lshl_add_u64 v[2:3], v[2:3], 1, s[6:7]
	v_lshl_add_u64 v[22:23], v[2:3], 0, v[0:1]
	v_add_u32_e32 v2, 32, v4
	v_min_i32_e32 v2, s25, v2
	v_mad_i64_i32 v[2:3], s[0:1], v2, s10, 0
	v_lshl_add_u64 v[2:3], v[2:3], 1, s[4:5]
	v_lshl_add_u64 v[24:25], v[2:3], 0, v[0:1]
	v_add_u32_e32 v2, 32, v5
	v_min_i32_e32 v2, s24, v2
	v_mad_i64_i32 v[2:3], s[0:1], v2, s10, 0
	v_lshl_add_u64 v[2:3], v[2:3], 1, s[6:7]
	v_lshl_add_u64 v[26:27], v[2:3], 0, v[0:1]
	v_add_u32_e32 v2, 48, v4
	v_min_i32_e32 v2, s25, v2
	v_mad_i64_i32 v[2:3], s[0:1], v2, s10, 0
	v_lshl_add_u64 v[2:3], v[2:3], 1, s[4:5]
	v_lshl_add_u64 v[28:29], v[2:3], 0, v[0:1]
	v_add_u32_e32 v2, 48, v5
	v_min_i32_e32 v2, s24, v2
	v_mad_i64_i32 v[2:3], s[0:1], v2, s10, 0
	v_add_u32_e32 v37, s26, v36
	s_add_i32 s18, s11, -8
	v_lshl_add_u64 v[2:3], v[2:3], 1, s[6:7]
	v_lshl_add_u64 v[30:31], v[2:3], 0, v[0:1]
	v_min_i32_e32 v0, s18, v37
	v_sub_u32_e32 v0, v0, v36
	v_ashrrev_i32_e32 v1, 31, v0
	v_lshlrev_b64 v[8:9], 1, v[0:1]
	v_lshl_add_u64 v[0:1], v[18:19], 0, v[8:9]
	v_lshl_add_u64 v[2:3], v[22:23], 0, v[8:9]
	global_load_dwordx4 v[54:57], v[0:1], off
	global_load_dwordx4 v[58:61], v[2:3], off
	v_lshl_add_u64 v[0:1], v[26:27], 0, v[8:9]
	v_lshl_add_u64 v[2:3], v[30:31], 0, v[8:9]
	v_lshl_add_u64 v[10:11], v[16:17], 0, v[8:9]
	v_lshl_add_u64 v[12:13], v[20:21], 0, v[8:9]
	v_lshl_add_u64 v[40:41], v[24:25], 0, v[8:9]
	global_load_dwordx4 v[62:65], v[0:1], off
	global_load_dwordx4 v[66:69], v[2:3], off
	s_nop 0
	global_load_dwordx4 v[0:3], v[10:11], off
	global_load_dwordx4 v[4:7], v[12:13], off
	v_lshl_add_u64 v[42:43], v[28:29], 0, v[8:9]
	global_load_dwordx4 v[8:11], v[40:41], off
	global_load_dwordx4 v[12:15], v[42:43], off
	v_accvgpr_write_b32 a0, 0
	v_mul_u32_u24_e32 v38, 0xa8, v38
	v_or_b32_e32 v43, v34, v33
	v_mul_u32_u24_e32 v40, 0xa8, v44
	v_accvgpr_mov_b32 a3, a0
	v_add_lshl_u32 v38, v38, v39, 1
	s_movk_i32 s4, 0x5400
	v_or_b32_e32 v42, v35, v33
	v_add_lshl_u32 v40, v40, v36, 1
	s_movk_i32 s5, 0x150
	v_mul_u32_u24_e32 v43, 0x150, v43
	v_lshlrev_b32_e32 v44, 4, v32
	v_accvgpr_mov_b32 a1, a0
	v_accvgpr_mov_b32 a2, a0
	v_accvgpr_mov_b32 a7, a3
	v_accvgpr_mov_b32 a11, a3
	v_accvgpr_mov_b32 a15, a3
	v_cmp_gt_i32_e64 s[0:1], s11, v37
	s_add_i32 s6, s23, -1
	v_add_u32_e32 v39, 0x5400, v38
	v_add_u32_e32 v41, 0x5400, v40
	v_mad_u32_u24 v42, v42, s5, v44
	v_add3_u32 v43, v43, v44, s4
	s_mov_b32 s7, 0
	v_accvgpr_mov_b32 a6, a2
	v_accvgpr_mov_b32 a5, a1
	v_accvgpr_mov_b32 a4, a0
	v_accvgpr_mov_b32 a10, a2
	v_accvgpr_mov_b32 a9, a1
	v_accvgpr_mov_b32 a8, a0
	v_accvgpr_mov_b32 a14, a2
	v_accvgpr_mov_b32 a13, a1
	v_accvgpr_mov_b32 a12, a0
	v_mov_b32_e32 v86, 0
	v_mov_b32_e32 v87, 0
	v_mov_b32_e32 v138, 0
	v_mov_b32_e32 v139, 0
	s_cmp_lg_u32 s21, 0
	s_cbranch_scc1 .Lgf16_nobias
	v_or3_b32 v136, v34, s22, v33
	v_or_b32_e32 v137, 16, v136
	s_movk_i32 s24, 0x12c
	v_cmp_gt_i32_e32 vcc, s9, v136
	s_and_saveexec_b64 s[0:1], vcc
	v_lshlrev_b32_e32 v140, 2, v136
	global_load_dword v86, v140, s[12:13]
	v_add_u32_e32 v141, 0xfffffe3e, v136
	v_cmp_gt_u32_e32 vcc, s24, v136
	v_cmp_gt_u32_e64 s[24:25], s24, v141
	s_or_b64 s[24:25], s[24:25], vcc
	s_and_b64 exec, exec, s[24:25]
	global_load_dword v138, v140, s[14:15]
	s_or_b64 exec, exec, s[0:1]
	s_movk_i32 s24, 0x12c
	v_cmp_gt_i32_e32 vcc, s9, v137
	s_and_saveexec_b64 s[0:1], vcc
	v_lshlrev_b32_e32 v140, 2, v137
	global_load_dword v87, v140, s[12:13]
	v_add_u32_e32 v141, 0xfffffe3e, v137
	v_cmp_gt_u32_e32 vcc, s24, v137
	v_cmp_gt_u32_e64 s[24:25], s24, v141
	s_or_b64 s[24:25], s[24:25], vcc
	s_and_b64 exec, exec, s[24:25]
	global_load_dword v139, v140, s[14:15]
	s_or_b64 exec, exec, s[0:1]
	s_movk_i32 s24, 0x12c
.Lgf16_nobias:
	v_min_i32_e32 v44, s18, v37
	v_sub_u32_e32 v44, v44, v36
	v_ashrrev_i32_e32 v45, 31, v44
	v_lshlrev_b64 v[44:45], 1, v[44:45]
	v_lshl_add_u64 v[18:19], v[18:19], 0, v[44:45]
	v_lshl_add_u64 v[22:23], v[22:23], 0, v[44:45]
	v_lshl_add_u64 v[26:27], v[26:27], 0, v[44:45]
	v_lshl_add_u64 v[30:31], v[30:31], 0, v[44:45]
	v_lshl_add_u64 v[16:17], v[16:17], 0, v[44:45]
	v_lshl_add_u64 v[20:21], v[20:21], 0, v[44:45]
	v_lshl_add_u64 v[24:25], v[24:25], 0, v[44:45]
	v_lshl_add_u64 v[28:29], v[28:29], 0, v[44:45]
	global_load_dwordx4 v[104:107], v[18:19], off offset:256
	global_load_dwordx4 v[108:111], v[22:23], off offset:256
	global_load_dwordx4 v[112:115], v[26:27], off offset:256
	global_load_dwordx4 v[116:119], v[30:31], off offset:256
	global_load_dwordx4 v[88:91], v[16:17], off offset:256
	global_load_dwordx4 v[92:95], v[20:21], off offset:256
	global_load_dwordx4 v[96:99], v[24:25], off offset:256
	global_load_dwordx4 v[100:103], v[28:29], off offset:256
	s_waitcnt vmcnt(14)
	ds_write_b128 v41, v[54:57]
	ds_write_b128 v41, v[58:61] offset:5376
	s_waitcnt vmcnt(12)
	ds_write_b128 v41, v[62:65] offset:10752
	ds_write_b128 v41, v[66:69] offset:16128
	s_waitcnt vmcnt(10)
	ds_write_b128 v40, v[0:3]
	ds_write_b128 v40, v[4:7] offset:5376
	s_waitcnt vmcnt(8)
	ds_write_b128 v40, v[8:11] offset:10752
	ds_write_b128 v40, v[12:15] offset:16128
	s_waitcnt lgkmcnt(0)
	global_load_dwordx4 v[54:57], v[18:19], off offset:512
	global_load_dwordx4 v[58:61], v[22:23], off offset:512
	global_load_dwordx4 v[62:65], v[26:27], off offset:512
	global_load_dwordx4 v[66:69], v[30:31], off offset:512
	global_load_dwordx4 v[0:3], v[16:17], off offset:512
	global_load_dwordx4 v[4:7], v[20:21], off offset:512
	global_load_dwordx4 v[8:11], v[24:25], off offset:512
	global_load_dwordx4 v[12:15], v[28:29], off offset:512
	s_barrier
	ds_read_b128 v[70:73], v42
	ds_read_b128 v[74:77], v43
	ds_read_b128 v[78:81], v42 offset:5376
	ds_read_b128 v[82:85], v43 offset:5376
	ds_read_b128 v[120:123], v42 offset:64
	ds_read_b128 v[124:127], v43 offset:64
	ds_read_b128 v[128:131], v42 offset:5440
	ds_read_b128 v[132:135], v43 offset:5440
	s_waitcnt lgkmcnt(6)
	v_mfma_f32_16x16x32_f16 a[12:15], v[70:73], v[74:77], a[12:15]
	s_waitcnt lgkmcnt(4)
	v_mfma_f32_16x16x32_f16 a[8:11], v[70:73], v[82:85], a[8:11]
	v_mfma_f32_16x16x32_f16 a[4:7], v[78:81], v[74:77], a[4:7]
	v_mfma_f32_16x16x32_f16 a[0:3], v[78:81], v[82:85], a[0:3]
	ds_read_b128 v[70:73], v42 offset:128
	ds_read_b128 v[74:77], v43 offset:128
	ds_read_b128 v[78:81], v42 offset:5504
	ds_read_b128 v[82:85], v43 offset:5504
	s_waitcnt lgkmcnt(6)
	v_mfma_f32_16x16x32_f16 a[12:15], v[120:123], v[124:127], a[12:15]
	s_waitcnt lgkmcnt(4)
	v_mfma_f32_16x16x32_f16 a[8:11], v[120:123], v[132:135], a[8:11]
	v_mfma_f32_16x16x32_f16 a[4:7], v[128:131], v[124:127], a[4:7]
	v_mfma_f32_16x16x32_f16 a[0:3], v[128:131], v[132:135], a[0:3]
	ds_read_b128 v[120:123], v42 offset:192
	ds_read_b128 v[124:127], v43 offset:192
	ds_read_b128 v[128:131], v42 offset:5568
	ds_read_b128 v[132:135], v43 offset:5568
	s_waitcnt lgkmcnt(6)
	v_mfma_f32_16x16x32_f16 a[12:15], v[70:73], v[74:77], a[12:15]
	s_waitcnt lgkmcnt(4)
	v_mfma_f32_16x16x32_f16 a[8:11], v[70:73], v[82:85], a[8:11]
	v_mfma_f32_16x16x32_f16 a[4:7], v[78:81], v[74:77], a[4:7]
	v_mfma_f32_16x16x32_f16 a[0:3], v[78:81], v[82:85], a[0:3]
	s_waitcnt lgkmcnt(2)
	v_mfma_f32_16x16x32_f16 a[12:15], v[120:123], v[124:127], a[12:15]
	s_waitcnt lgkmcnt(0)
	v_mfma_f32_16x16x32_f16 a[8:11], v[120:123], v[132:135], a[8:11]
	v_mfma_f32_16x16x32_f16 a[4:7], v[128:131], v[124:127], a[4:7]
	v_mfma_f32_16x16x32_f16 a[0:3], v[128:131], v[132:135], a[0:3]
	s_barrier
	s_waitcnt vmcnt(14)
	ds_write_b128 v41, v[104:107]
	ds_write_b128 v41, v[108:111] offset:5376
	s_waitcnt vmcnt(12)
	ds_write_b128 v41, v[112:115] offset:10752
	ds_write_b128 v41, v[116:119] offset:16128
	s_waitcnt vmcnt(10)
	ds_write_b128 v40, v[88:91]
	ds_write_b128 v40, v[92:95] offset:5376
	s_waitcnt vmcnt(8)
	ds_write_b128 v40, v[96:99] offset:10752
	ds_write_b128 v40, v[100:103] offset:16128
	s_waitcnt lgkmcnt(0)
	global_load_dwordx4 v[104:107], v[18:19], off offset:768
	global_load_dwordx4 v[108:111], v[22:23], off offset:768
	global_load_dwordx4 v[112:115], v[26:27], off offset:768
	global_load_dwordx4 v[116:119], v[30:31], off offset:768
	global_load_dwordx4 v[88:91], v[16:17], off offset:768
	global_load_dwordx4 v[92:95], v[20:21], off offset:768
	global_load_dwordx4 v[96:99], v[24:25], off offset:768
	global_load_dwordx4 v[100:103], v[28:29], off offset:768
	s_barrier
	ds_read_b128 v[70:73], v42
	ds_read_b128 v[74:77], v43
	ds_read_b128 v[78:81], v42 offset:5376
	ds_read_b128 v[82:85], v43 offset:5376
	ds_read_b128 v[120:123], v42 offset:64
	ds_read_b128 v[124:127], v43 offset:64
	ds_read_b128 v[128:131], v42 offset:5440
	ds_read_b128 v[132:135], v43 offset:5440
	s_waitcnt lgkmcnt(6)
	v_mfma_f32_16x16x32_f16 a[12:15], v[70:73], v[74:77], a[12:15]
	s_waitcnt lgkmcnt(4)
	v_mfma_f32_16x16x32_f16 a[8:11], v[70:73], v[82:85], a[8:11]
	v_mfma_f32_16x16x32_f16 a[4:7], v[78:81], v[74:77], a[4:7]
	v_mfma_f32_16x16x32_f16 a[0:3], v[78:81], v[82:85], a[0:3]
	ds_read_b128 v[70:73], v42 offset:128
	ds_read_b128 v[74:77], v43 offset:128
	ds_read_b128 v[78:81], v42 offset:5504
	ds_read_b128 v[82:85], v43 offset:5504
	s_waitcnt lgkmcnt(6)
	v_mfma_f32_16x16x32_f16 a[12:15], v[120:123], v[124:127], a[12:15]
	s_waitcnt lgkmcnt(4)
	v_mfma_f32_16x16x32_f16 a[8:11], v[120:123], v[132:135], a[8:11]
	v_mfma_f32_16x16x32_f16 a[4:7], v[128:131], v[124:127], a[4:7]
	v_mfma_f32_16x16x32_f16 a[0:3], v[128:131], v[132:135], a[0:3]
	ds_read_b128 v[120:123], v42 offset:192
	ds_read_b128 v[124:127], v43 offset:192
	ds_read_b128 v[128:131], v42 offset:5568
	ds_read_b128 v[132:135], v43 offset:5568
	s_waitcnt lgkmcnt(6)
	v_mfma_f32_16x16x32_f16 a[12:15], v[70:73], v[74:77], a[12:15]
	s_waitcnt lgkmcnt(4)
	v_mfma_f32_16x16x32_f16 a[8:11], v[70:73], v[82:85], a[8:11]
	v_mfma_f32_16x16x32_f16 a[4:7], v[78:81], v[74:77], a[4:7]
	v_mfma_f32_16x16x32_f16 a[0:3], v[78:81], v[82:85], a[0:3]
	s_waitcnt lgkmcnt(2)
	v_mfma_f32_16x16x32_f16 a[12:15], v[120:123], v[124:127], a[12:15]
	s_waitcnt lgkmcnt(0)
	v_mfma_f32_16x16x32_f16 a[8:11], v[120:123], v[132:135], a[8:11]
	v_mfma_f32_16x16x32_f16 a[4:7], v[128:131], v[124:127], a[4:7]
	v_mfma_f32_16x16x32_f16 a[0:3], v[128:131], v[132:135], a[0:3]
	s_barrier
	s_waitcnt vmcnt(14)
	ds_write_b128 v41, v[54:57]
	ds_write_b128 v41, v[58:61] offset:5376
	s_waitcnt vmcnt(12)
	ds_write_b128 v41, v[62:65] offset:10752
	ds_write_b128 v41, v[66:69] offset:16128
	s_waitcnt vmcnt(10)
	ds_write_b128 v40, v[0:3]
	ds_write_b128 v40, v[4:7] offset:5376
	s_waitcnt vmcnt(8)
	ds_write_b128 v40, v[8:11] offset:10752
	ds_write_b128 v40, v[12:15] offset:16128
	s_waitcnt lgkmcnt(0)
	global_load_dwordx4 v[54:57], v[18:19], off offset:1024
	global_load_dwordx4 v[58:61], v[22:23], off offset:1024
	global_load_dwordx4 v[62:65], v[26:27], off offset:1024
	global_load_dwordx4 v[66:69], v[30:31], off offset:1024
	global_load_dwordx4 v[0:3], v[16:17], off offset:1024
	global_load_dwordx4 v[4:7], v[20:21], off offset:1024
	global_load_dwordx4 v[8:11], v[24:25], off offset:1024
	global_load_dwordx4 v[12:15], v[28:29], off offset:1024
	s_barrier
	ds_read_b128 v[70:73], v42
	ds_read_b128 v[74:77], v43
	ds_read_b128 v[78:81], v42 offset:5376
	ds_read_b128 v[82:85], v43 offset:5376
	ds_read_b128 v[120:123], v42 offset:64
	ds_read_b128 v[124:127], v43 offset:64
	ds_read_b128 v[128:131], v42 offset:5440
	ds_read_b128 v[132:135], v43 offset:5440
	s_waitcnt lgkmcnt(6)
	v_mfma_f32_16x16x32_f16 a[12:15], v[70:73], v[74:77], a[12:15]
	s_waitcnt lgkmcnt(4)
	v_mfma_f32_16x16x32_f16 a[8:11], v[70:73], v[82:85], a[8:11]
	v_mfma_f32_16x16x32_f16 a[4:7], v[78:81], v[74:77], a[4:7]
	v_mfma_f32_16x16x32_f16 a[0:3], v[78:81], v[82:85], a[0:3]
	ds_read_b128 v[70:73], v42 offset:128
	ds_read_b128 v[74:77], v43 offset:128
	ds_read_b128 v[78:81], v42 offset:5504
	ds_read_b128 v[82:85], v43 offset:5504
	s_waitcnt lgkmcnt(6)
	v_mfma_f32_16x16x32_f16 a[12:15], v[120:123], v[124:127], a[12:15]
	s_waitcnt lgkmcnt(4)
	v_mfma_f32_16x16x32_f16 a[8:11], v[120:123], v[132:135], a[8:11]
	v_mfma_f32_16x16x32_f16 a[4:7], v[128:131], v[124:127], a[4:7]
	v_mfma_f32_16x16x32_f16 a[0:3], v[128:131], v[132:135], a[0:3]
	ds_read_b128 v[120:123], v42 offset:192
	ds_read_b128 v[124:127], v43 offset:192
	ds_read_b128 v[128:131], v42 offset:5568
	ds_read_b128 v[132:135], v43 offset:5568
	s_waitcnt lgkmcnt(6)
	v_mfma_f32_16x16x32_f16 a[12:15], v[70:73], v[74:77], a[12:15]
	s_waitcnt lgkmcnt(4)
	v_mfma_f32_16x16x32_f16 a[8:11], v[70:73], v[82:85], a[8:11]
	v_mfma_f32_16x16x32_f16 a[4:7], v[78:81], v[74:77], a[4:7]
	v_mfma_f32_16x16x32_f16 a[0:3], v[78:81], v[82:85], a[0:3]
	s_waitcnt lgkmcnt(2)
	v_mfma_f32_16x16x32_f16 a[12:15], v[120:123], v[124:127], a[12:15]
	s_waitcnt lgkmcnt(0)
	v_mfma_f32_16x16x32_f16 a[8:11], v[120:123], v[132:135], a[8:11]
	v_mfma_f32_16x16x32_f16 a[4:7], v[128:131], v[124:127], a[4:7]
	v_mfma_f32_16x16x32_f16 a[0:3], v[128:131], v[132:135], a[0:3]
	s_barrier
	s_waitcnt vmcnt(14)
	ds_write_b128 v41, v[104:107]
	ds_write_b128 v41, v[108:111] offset:5376
	s_waitcnt vmcnt(12)
	ds_write_b128 v41, v[112:115] offset:10752
	ds_write_b128 v41, v[116:119] offset:16128
	s_waitcnt vmcnt(10)
	ds_write_b128 v40, v[88:91]
	ds_write_b128 v40, v[92:95] offset:5376
	s_waitcnt vmcnt(8)
	ds_write_b128 v40, v[96:99] offset:10752
	ds_write_b128 v40, v[100:103] offset:16128
	s_waitcnt lgkmcnt(0)
	global_load_dwordx4 v[104:107], v[18:19], off offset:1280
	global_load_dwordx4 v[108:111], v[22:23], off offset:1280
	global_load_dwordx4 v[112:115], v[26:27], off offset:1280
	global_load_dwordx4 v[116:119], v[30:31], off offset:1280
	global_load_dwordx4 v[88:91], v[16:17], off offset:1280
	global_load_dwordx4 v[92:95], v[20:21], off offset:1280
	global_load_dwordx4 v[96:99], v[24:25], off offset:1280
	global_load_dwordx4 v[100:103], v[28:29], off offset:1280
	s_barrier
	ds_read_b128 v[70:73], v42
	ds_read_b128 v[74:77], v43
	ds_read_b128 v[78:81], v42 offset:5376
	ds_read_b128 v[82:85], v43 offset:5376
	ds_read_b128 v[120:123], v42 offset:64
	ds_read_b128 v[124:127], v43 offset:64
	ds_read_b128 v[128:131], v42 offset:5440
	ds_read_b128 v[132:135], v43 offset:5440
	s_waitcnt lgkmcnt(6)
	v_mfma_f32_16x16x32_f16 a[12:15], v[70:73], v[74:77], a[12:15]
	s_waitcnt lgkmcnt(4)
	v_mfma_f32_16x16x32_f16 a[8:11], v[70:73], v[82:85], a[8:11]
	v_mfma_f32_16x16x32_f16 a[4:7], v[78:81], v[74:77], a[4:7]
	v_mfma_f32_16x16x32_f16 a[0:3], v[78:81], v[82:85], a[0:3]
	ds_read_b128 v[70:73], v42 offset:128
	ds_read_b128 v[74:77], v43 offset:128
	ds_read_b128 v[78:81], v42 offset:5504
	ds_read_b128 v[82:85], v43 offset:5504
	s_waitcnt lgkmcnt(6)
	v_mfma_f32_16x16x32_f16 a[12:15], v[120:123], v[124:127], a[12:15]
	s_waitcnt lgkmcnt(4)
	v_mfma_f32_16x16x32_f16 a[8:11], v[120:123], v[132:135], a[8:11]
	v_mfma_f32_16x16x32_f16 a[4:7], v[128:131], v[124:127], a[4:7]
	v_mfma_f32_16x16x32_f16 a[0:3], v[128:131], v[132:135], a[0:3]
	ds_read_b128 v[120:123], v42 offset:192
	ds_read_b128 v[124:127], v43 offset:192
	ds_read_b128 v[128:131], v42 offset:5568
	ds_read_b128 v[132:135], v43 offset:5568
	s_waitcnt lgkmcnt(6)
	v_mfma_f32_16x16x32_f16 a[12:15], v[70:73], v[74:77], a[12:15]
	s_waitcnt lgkmcnt(4)
	v_mfma_f32_16x16x32_f16 a[8:11], v[70:73], v[82:85], a[8:11]
	v_mfma_f32_16x16x32_f16 a[4:7], v[78:81], v[74:77], a[4:7]
	v_mfma_f32_16x16x32_f16 a[0:3], v[78:81], v[82:85], a[0:3]
	s_waitcnt lgkmcnt(2)
	v_mfma_f32_16x16x32_f16 a[12:15], v[120:123], v[124:127], a[12:15]
	s_waitcnt lgkmcnt(0)
	v_mfma_f32_16x16x32_f16 a[8:11], v[120:123], v[132:135], a[8:11]
	v_mfma_f32_16x16x32_f16 a[4:7], v[128:131], v[124:127], a[4:7]
	v_mfma_f32_16x16x32_f16 a[0:3], v[128:131], v[132:135], a[0:3]
	s_barrier
	s_waitcnt vmcnt(14)
	ds_write_b128 v41, v[54:57]
	ds_write_b128 v41, v[58:61] offset:5376
	s_waitcnt vmcnt(12)
	ds_write_b128 v41, v[62:65] offset:10752
	ds_write_b128 v41, v[66:69] offset:16128
	s_waitcnt vmcnt(10)
	ds_write_b128 v40, v[0:3]
	ds_write_b128 v40, v[4:7] offset:5376
	s_waitcnt vmcnt(8)
	ds_write_b128 v40, v[8:11] offset:10752
	ds_write_b128 v40, v[12:15] offset:16128
	s_waitcnt lgkmcnt(0)
	global_load_dwordx4 v[54:57], v[18:19], off offset:1536
	global_load_dwordx4 v[58:61], v[22:23], off offset:1536
	global_load_dwordx4 v[62:65], v[26:27], off offset:1536
	global_load_dwordx4 v[66:69], v[30:31], off offset:1536
	global_load_dwordx4 v[0:3], v[16:17], off offset:1536
	global_load_dwordx4 v[4:7], v[20:21], off offset:1536
	global_load_dwordx4 v[8:11], v[24:25], off offset:1536
	global_load_dwordx4 v[12:15], v[28:29], off offset:1536
	s_barrier
	ds_read_b128 v[70:73], v42
	ds_read_b128 v[74:77], v43
	ds_read_b128 v[78:81], v42 offset:5376
	ds_read_b128 v[82:85], v43 offset:5376
	ds_read_b128 v[120:123], v42 offset:64
	ds_read_b128 v[124:127], v43 offset:64
	ds_read_b128 v[128:131], v42 offset:5440
	ds_read_b128 v[132:135], v43 offset:5440
	s_waitcnt lgkmcnt(6)
	v_mfma_f32_16x16x32_f16 a[12:15], v[70:73], v[74:77], a[12:15]
	s_waitcnt lgkmcnt(4)
	v_mfma_f32_16x16x32_f16 a[8:11], v[70:73], v[82:85], a[8:11]
	v_mfma_f32_16x16x32_f16 a[4:7], v[78:81], v[74:77], a[4:7]
	v_mfma_f32_16x16x32_f16 a[0:3], v[78:81], v[82:85], a[0:3]
	ds_read_b128 v[70:73], v42 offset:128
	ds_read_b128 v[74:77], v43 offset:128
	ds_read_b128 v[78:81], v42 offset:5504
	ds_read_b128 v[82:85], v43 offset:5504
	s_waitcnt lgkmcnt(6)
	v_mfma_f32_16x16x32_f16 a[12:15], v[120:123], v[124:127], a[12:15]
	s_waitcnt lgkmcnt(4)
	v_mfma_f32_16x16x32_f16 a[8:11], v[120:123], v[132:135], a[8:11]
	v_mfma_f32_16x16x32_f16 a[4:7], v[128:131], v[124:127], a[4:7]
	v_mfma_f32_16x16x32_f16 a[0:3], v[128:131], v[132:135], a[0:3]
	ds_read_b128 v[120:123], v42 offset:192
	ds_read_b128 v[124:127], v43 offset:192
	ds_read_b128 v[128:131], v42 offset:5568
	ds_read_b128 v[132:135], v43 offset:5568
	s_waitcnt lgkmcnt(6)
	v_mfma_f32_16x16x32_f16 a[12:15], v[70:73], v[74:77], a[12:15]
	s_waitcnt lgkmcnt(4)
	v_mfma_f32_16x16x32_f16 a[8:11], v[70:73], v[82:85], a[8:11]
	v_mfma_f32_16x16x32_f16 a[4:7], v[78:81], v[74:77], a[4:7]
	v_mfma_f32_16x16x32_f16 a[0:3], v[78:81], v[82:85], a[0:3]
	s_waitcnt lgkmcnt(2)
	v_mfma_f32_16x16x32_f16 a[12:15], v[120:123], v[124:127], a[12:15]
	s_waitcnt lgkmcnt(0)
	v_mfma_f32_16x16x32_f16 a[8:11], v[120:123], v[132:135], a[8:11]
	v_mfma_f32_16x16x32_f16 a[4:7], v[128:131], v[124:127], a[4:7]
	v_mfma_f32_16x16x32_f16 a[0:3], v[128:131], v[132:135], a[0:3]
	s_barrier
	s_waitcnt vmcnt(14)
	ds_write_b128 v41, v[104:107]
	ds_write_b128 v41, v[108:111] offset:5376
	s_waitcnt vmcnt(12)
	ds_write_b128 v41, v[112:115] offset:10752
	ds_write_b128 v41, v[116:119] offset:16128
	s_waitcnt vmcnt(10)
	ds_write_b128 v40, v[88:91]
	ds_write_b128 v40, v[92:95] offset:5376
	s_waitcnt vmcnt(8)
	ds_write_b128 v40, v[96:99] offset:10752
	ds_write_b128 v40, v[100:103] offset:16128
	s_waitcnt lgkmcnt(0)
	s_barrier
	ds_read_b128 v[70:73], v42
	ds_read_b128 v[74:77], v43
	ds_read_b128 v[78:81], v42 offset:5376
	ds_read_b128 v[82:85], v43 offset:5376
	ds_read_b128 v[120:123], v42 offset:64
	ds_read_b128 v[124:127], v43 offset:64
	ds_read_b128 v[128:131], v42 offset:5440
	ds_read_b128 v[132:135], v43 offset:5440
	s_waitcnt lgkmcnt(6)
	v_mfma_f32_16x16x32_f16 a[12:15], v[70:73], v[74:77], a[12:15]
	s_waitcnt lgkmcnt(4)
	v_mfma_f32_16x16x32_f16 a[8:11], v[70:73], v[82:85], a[8:11]
	v_mfma_f32_16x16x32_f16 a[4:7], v[78:81], v[74:77], a[4:7]
	v_mfma_f32_16x16x32_f16 a[0:3], v[78:81], v[82:85], a[0:3]
	ds_read_b128 v[70:73], v42 offset:128
	ds_read_b128 v[74:77], v43 offset:128
	ds_read_b128 v[78:81], v42 offset:5504
	ds_read_b128 v[82:85], v43 offset:5504
	s_waitcnt lgkmcnt(6)
	v_mfma_f32_16x16x32_f16 a[12:15], v[120:123], v[124:127], a[12:15]
	s_waitcnt lgkmcnt(4)
	v_mfma_f32_16x16x32_f16 a[8:11], v[120:123], v[132:135], a[8:11]
	v_mfma_f32_16x16x32_f16 a[4:7], v[128:131], v[124:127], a[4:7]
	v_mfma_f32_16x16x32_f16 a[0:3], v[128:131], v[132:135], a[0:3]
	ds_read_b128 v[120:123], v42 offset:192
	ds_read_b128 v[124:127], v43 offset:192
	ds_read_b128 v[128:131], v42 offset:5568
	ds_read_b128 v[132:135], v43 offset:5568
	s_waitcnt lgkmcnt(6)
	v_mfma_f32_16x16x32_f16 a[12:15], v[70:73], v[74:77], a[12:15]
	s_waitcnt lgkmcnt(4)
	v_mfma_f32_16x16x32_f16 a[8:11], v[70:73], v[82:85], a[8:11]
	v_mfma_f32_16x16x32_f16 a[4:7], v[78:81], v[74:77], a[4:7]
	v_mfma_f32_16x16x32_f16 a[0:3], v[78:81], v[82:85], a[0:3]
	s_waitcnt lgkmcnt(2)
	v_mfma_f32_16x16x32_f16 a[12:15], v[120:123], v[124:127], a[12:15]
	s_waitcnt lgkmcnt(0)
	v_mfma_f32_16x16x32_f16 a[8:11], v[120:123], v[132:135], a[8:11]
	v_mfma_f32_16x16x32_f16 a[4:7], v[128:131], v[124:127], a[4:7]
	v_mfma_f32_16x16x32_f16 a[0:3], v[128:131], v[132:135], a[0:3]
	s_barrier
	s_waitcnt vmcnt(6)
	ds_write_b128 v41, v[54:57]
	ds_write_b128 v41, v[58:61] offset:5376
	s_waitcnt vmcnt(4)
	ds_write_b128 v41, v[62:65] offset:10752
	ds_write_b128 v41, v[66:69] offset:16128
	s_waitcnt vmcnt(2)
	ds_write_b128 v40, v[0:3]
	ds_write_b128 v40, v[4:7] offset:5376
	s_waitcnt vmcnt(0)
	ds_write_b128 v40, v[8:11] offset:10752
	ds_write_b128 v40, v[12:15] offset:16128
	ds_write_b128 v38, v[46:49] offset:256
	ds_write_b128 v39, v[50:53] offset:256
	s_waitcnt lgkmcnt(0)
	s_barrier
	ds_read_b128 v[70:73], v42
	ds_read_b128 v[74:77], v43
	ds_read_b128 v[78:81], v42 offset:5376
	ds_read_b128 v[82:85], v43 offset:5376
	ds_read_b128 v[120:123], v42 offset:64
	ds_read_b128 v[124:127], v43 offset:64
	ds_read_b128 v[128:131], v42 offset:5440
	ds_read_b128 v[132:135], v43 offset:5440
	s_waitcnt lgkmcnt(6)
	v_mfma_f32_16x16x32_f16 a[12:15], v[70:73], v[74:77], a[12:15]
	s_waitcnt lgkmcnt(4)
	v_mfma_f32_16x16x32_f16 a[8:11], v[70:73], v[82:85], a[8:11]
	v_mfma_f32_16x16x32_f16 a[4:7], v[78:81], v[74:77], a[4:7]
	v_mfma_f32_16x16x32_f16 a[0:3], v[78:81], v[82:85], a[0:3]
	ds_read_b128 v[70:73], v42 offset:128
	ds_read_b128 v[74:77], v43 offset:128
	ds_read_b128 v[78:81], v42 offset:5504
	ds_read_b128 v[82:85], v43 offset:5504
	s_waitcnt lgkmcnt(6)
	v_mfma_f32_16x16x32_f16 a[12:15], v[120:123], v[124:127], a[12:15]
	s_waitcnt lgkmcnt(4)
	v_mfma_f32_16x16x32_f16 a[8:11], v[120:123], v[132:135], a[8:11]
	v_mfma_f32_16x16x32_f16 a[4:7], v[128:131], v[124:127], a[4:7]
	v_mfma_f32_16x16x32_f16 a[0:3], v[128:131], v[132:135], a[0:3]
	ds_read_b128 v[120:123], v42 offset:192
	ds_read_b128 v[124:127], v43 offset:192
	ds_read_b128 v[128:131], v42 offset:5568
	ds_read_b128 v[132:135], v43 offset:5568
	s_waitcnt lgkmcnt(6)
	v_mfma_f32_16x16x32_f16 a[12:15], v[70:73], v[74:77], a[12:15]
	s_waitcnt lgkmcnt(4)
	v_mfma_f32_16x16x32_f16 a[8:11], v[70:73], v[82:85], a[8:11]
	v_mfma_f32_16x16x32_f16 a[4:7], v[78:81], v[74:77], a[4:7]
	v_mfma_f32_16x16x32_f16 a[0:3], v[78:81], v[82:85], a[0:3]
	ds_read_b128 v[70:73], v42 offset:256
	ds_read_b128 v[74:77], v43 offset:256
	ds_read_b128 v[78:81], v42 offset:5632
	ds_read_b128 v[82:85], v43 offset:5632
	s_waitcnt lgkmcnt(6)
	v_mfma_f32_16x16x32_f16 a[12:15], v[120:123], v[124:127], a[12:15]
	s_waitcnt lgkmcnt(4)
	v_mfma_f32_16x16x32_f16 a[8:11], v[120:123], v[132:135], a[8:11]
	v_mfma_f32_16x16x32_f16 a[4:7], v[128:131], v[124:127], a[4:7]
	v_mfma_f32_16x16x32_f16 a[0:3], v[128:131], v[132:135], a[0:3]
	s_waitcnt lgkmcnt(2)
	v_mfma_f32_16x16x32_f16 a[12:15], v[70:73], v[74:77], a[12:15]
	s_waitcnt lgkmcnt(0)
	v_mfma_f32_16x16x32_f16 a[8:11], v[70:73], v[82:85], a[8:11]
	v_mfma_f32_16x16x32_f16 a[4:7], v[78:81], v[74:77], a[4:7]
	v_mfma_f32_16x16x32_f16 a[0:3], v[78:81], v[82:85], a[0:3]
	s_barrier
	s_waitcnt vmcnt(0)
	v_add_f32_e32 v86, v86, v138
	v_add_f32_e32 v87, v87, v139
	v_mov_b32_e32 v3, v34
	v_mov_b32_e32 v2, v35
.LBB0_16:
	s_ashr_i32 s0, s21, 31
	s_mul_i32 s2, s9, s8
	s_mul_hi_i32 s1, s9, s8
	s_mul_i32 s0, s2, s0
	s_mul_hi_u32 s3, s2, s21
	s_add_i32 s0, s3, s0
	s_mul_i32 s1, s1, s21
	s_add_i32 s1, s0, s1
	s_mul_i32 s0, s2, s21
	s_lshl_b64 s[0:1], s[0:1], 2
	s_waitcnt lgkmcnt(0)
	s_add_u32 s10, s16, s0
	s_addc_u32 s11, s17, s1
	s_cmp_eq_u32 s21, 0
	s_cselect_b64 s[0:1], -1, 0
	v_or3_b32 v0, v3, s22, v33
	s_cmp_lg_u32 s21, 0
	v_add_u32_e32 v1, s20, v2
	v_cndmask_b32_e64 v2, 0, 1, s[0:1]
	s_waitcnt vmcnt(3)
	v_accvgpr_read_b32 v7, a0
	v_accvgpr_read_b32 v6, a1
	v_accvgpr_read_b32 v5, a2
	v_accvgpr_read_b32 v4, a3
	s_waitcnt vmcnt(1)
	v_accvgpr_read_b32 v12, a4
	v_accvgpr_read_b32 v11, a5
	v_accvgpr_read_b32 v10, a6
	v_accvgpr_read_b32 v9, a7
	v_accvgpr_read_b32 v17, a8
	v_accvgpr_read_b32 v16, a9
	v_accvgpr_read_b32 v15, a10
	v_accvgpr_read_b32 v14, a11
	v_accvgpr_read_b32 v20, a12
	v_accvgpr_read_b32 v19, a13
	v_accvgpr_read_b32 v18, a14
	v_accvgpr_read_b32 v13, a15
	s_cselect_b64 s[4:5], -1, 0
	v_lshl_or_b32 v8, v32, 2, v1
	v_cmp_gt_i32_e64 s[2:3], s9, v0
	v_ashrrev_i32_e32 v1, 31, v0
	v_cmp_ne_u32_e64 s[0:1], 1, v2
	s_and_saveexec_b64 s[6:7], s[2:3]
	s_cbranch_execz .LBB0_29
	s_and_b64 vcc, exec, s[0:1]
	v_mov_b32_e32 v21, 0
	s_cbranch_vccnz .LBB0_21
	v_mov_b32_e32 v21, v86

.LBB0_33:
	v_mov_b32_e32 v18, v87

	.amdhsa_kernel _Z15gemm_f16_kernelPKDF16_S0_PKfS2_Pfiiiiiii
		.amdhsa_group_segment_fixed_size 43008
		.amdhsa_private_segment_fixed_size 0
		.amdhsa_kernarg_size 68
		.amdhsa_user_sgpr_count 2
		.amdhsa_user_sgpr_dispatch_ptr 0
		.amdhsa_user_sgpr_queue_ptr 0
		.amdhsa_user_sgpr_kernarg_segment_ptr 1
		.amdhsa_user_sgpr_dispatch_id 0
		.amdhsa_user_sgpr_kernarg_preload_length 0
		.amdhsa_user_sgpr_kernarg_preload_offset 0
		.amdhsa_user_sgpr_private_segment_size 0
		.amdhsa_uses_dynamic_stack 0
		.amdhsa_enable_private_segment 0
		.amdhsa_system_sgpr_workgroup_id_x 1
		.amdhsa_system_sgpr_workgroup_id_y 0
		.amdhsa_system_sgpr_workgroup_id_z 0
		.amdhsa_system_sgpr_workgroup_info 0
		.amdhsa_system_vgpr_workitem_id 0
		.amdhsa_next_free_vgpr 160
		.amdhsa_next_free_sgpr 96
		.amdhsa_accum_offset 144
		.amdhsa_reserve_vcc 1
		.amdhsa_float_round_mode_32 0
		.amdhsa_float_round_mode_16_64 0
		.amdhsa_float_denorm_mode_32 3
		.amdhsa_float_denorm_mode_16_64 3
		.amdhsa_dx10_clamp 1
		.amdhsa_ieee_mode 1
		.amdhsa_fp16_overflow 0
		.amdhsa_tg_split 0
		.amdhsa_exception_fp_ieee_invalid_op 0
		.amdhsa_exception_fp_denorm_src 0
		.amdhsa_exception_fp_ieee_div_zero 0
		.amdhsa_exception_fp_ieee_overflow 0
		.amdhsa_exception_fp_ieee_underflow 0
		.amdhsa_exception_fp_ieee_inexact 0
		.amdhsa_exception_int_div_zero 0
	.end_amdhsa_kernel

amdhsa.kernels:
  - .agpr_count:     16
    .args:
      - .actual_access:  read_only
        .address_space:  global
        .offset:         0
        .size:           8
        .value_kind:     global_buffer
      - .actual_access:  read_only
        .address_space:  global
        .offset:         8
        .size:           8
        .value_kind:     global_buffer
      - .actual_access:  read_only
        .address_space:  global
        .offset:         16
        .size:           8
        .value_kind:     global_buffer
      - .actual_access:  read_only
        .address_space:  global
        .offset:         24
        .size:           8
        .value_kind:     global_buffer
      - .actual_access:  write_only
        .address_space:  global
        .offset:         32
        .size:           8
        .value_kind:     global_buffer
      - .offset:         40
        .size:           4
        .value_kind:     by_value
      - .offset:         44
        .size:           4
        .value_kind:     by_value
      - .offset:         48
        .size:           4
        .value_kind:     by_value
      - .offset:         52
        .size:           4
        .value_kind:     by_value
      - .offset:         56
        .size:           4
        .value_kind:     by_value
      - .offset:         60
        .size:           4
        .value_kind:     by_value
      - .offset:         64
        .size:           4
        .value_kind:     by_value
    .group_segment_fixed_size: 43008
    .kernarg_segment_align: 8
    .kernarg_segment_size: 68
    .language:       OpenCL C
    .language_version:
      - 2
      - 0
    .max_flat_workgroup_size: 256
    .name:           _Z15gemm_f16_kernelPKDF16_S0_PKfS2_Pfiiiiiii
    .private_segment_fixed_size: 0
    .sgpr_count:     33
    .sgpr_spill_count: 0
    .symbol:         _Z15gemm_f16_kernelPKDF16_S0_PKfS2_Pfiiiiiii.kd
    .uniform_work_group_size: 1
    .uses_dynamic_stack: false
    .vgpr_count:     160
    .vgpr_spill_count: 0
    .wavefront_size: 64
  - .agpr_count:     0
    .args:
      - .actual_access:  read_only
        .address_space:  global
        .offset:         0
        .size:           8
        .value_kind:     global_buffer
      - .actual_access:  read_only
        .address_space:  global
        .offset:         8
        .size:           8
        .value_kind:     global_buffer
      - .actual_access:  read_only
        .address_space:  global
        .offset:         16
        .size:           8
        .value_kind:     global_buffer
      - .actual_access:  read_only
        .address_space:  global
        .offset:         24
        .size:           8
        .value_kind:     global_buffer
      - .actual_access:  read_only
        .address_space:  global
        .offset:         32
        .size:           8
        .value_kind:     global_buffer
      - .actual_access:  read_only
        .address_space:  global
        .offset:         40
        .size:           8
        .value_kind:     global_buffer
      - .actual_access:  write_only
        .address_space:  global
        .offset:         48
        .size:           8
        .value_kind:     global_buffer
      - .actual_access:  read_only
        .address_space:  global
        .offset:         56
        .size:           8
        .value_kind:     global_buffer
    .group_segment_fixed_size: 121472
    .kernarg_segment_align: 8
    .kernarg_segment_size: 64
    .language:       OpenCL C
    .language_version:
      - 2
      - 0
    .max_flat_workgroup_size: 512
    .name:           _Z15score_ds_kernelPKfS0_S0_S0_S0_S0_PfPKDF16_
    .private_segment_fixed_size: 0
    .sgpr_count:     32
    .sgpr_spill_count: 0
    .symbol:         _Z15score_ds_kernelPKfS0_S0_S0_S0_S0_PfPKDF16_.kd
    .uniform_work_group_size: 1
    .uses_dynamic_stack: false
    .vgpr_count:     256
    .vgpr_spill_count: 0
    .wavefront_size: 64
  - .agpr_count:     0
    .args:
      - .actual_access:  read_only
        .address_space:  global
        .offset:         0
        .size:           8
        .value_kind:     global_buffer
      - .actual_access:  read_only
        .address_space:  global
        .offset:         8
        .size:           8
        .value_kind:     global_buffer
      - .actual_access:  read_only
        .address_space:  global
        .offset:         16
        .size:           8
        .value_kind:     global_buffer
      - .actual_access:  read_only
        .address_space:  global
        .offset:         24
        .size:           8
        .value_kind:     global_buffer
      - .actual_access:  read_only
        .address_space:  global
        .offset:         32
        .size:           8
        .value_kind:     global_buffer
      - .actual_access:  read_only
        .address_space:  global
        .offset:         40
        .size:           8
        .value_kind:     global_buffer
      - .actual_access:  read_only
        .address_space:  global
        .offset:         48
        .size:           8
        .value_kind:     global_buffer
      - .actual_access:  read_only
        .address_space:  global
        .offset:         56
        .size:           8
        .value_kind:     global_buffer
      - .actual_access:  read_only
        .address_space:  global
        .offset:         64
        .size:           8
        .value_kind:     global_buffer
      - .actual_access:  read_only
        .address_space:  global
        .offset:         72
        .size:           8
        .value_kind:     global_buffer
      - .actual_access:  write_only
        .address_space:  global
        .offset:         80
        .size:           8
        .value_kind:     global_buffer
    .group_segment_fixed_size: 94336
    .kernarg_segment_align: 8
    .kernarg_segment_size: 88
    .language:       OpenCL C
    .language_version:
      - 2
      - 0
    .max_flat_workgroup_size: 1024
    .name:           _Z13attend_kernelPKfS0_S0_S0_S0_S0_S0_S0_S0_S0_PDF16_
    .private_segment_fixed_size: 0
    .sgpr_count:     40
    .sgpr_spill_count: 0
    .symbol:         _Z13attend_kernelPKfS0_S0_S0_S0_S0_S0_S0_S0_S0_PDF16_.kd
    .uniform_work_group_size: 1
    .uses_dynamic_stack: false
    .vgpr_count:     128
    .vgpr_spill_count: 0
    .wavefront_size: 64
  - .agpr_count:     0
    .args:
      - .actual_access:  read_only
        .address_space:  global
        .offset:         0
        .size:           8
        .value_kind:     global_buffer
      - .actual_access:  read_only
        .address_space:  global
        .offset:         8
        .size:           8
        .value_kind:     global_buffer
      - .actual_access:  read_only
        .address_space:  global
        .offset:         16
        .size:           8
        .value_kind:     global_buffer
      - .actual_access:  read_only
        .address_space:  global
        .offset:         24
        .size:           8
        .value_kind:     global_buffer
      - .actual_access:  write_only
        .address_space:  global
        .offset:         32
        .size:           8
        .value_kind:     global_buffer
    .group_segment_fixed_size: 9088
    .kernarg_segment_align: 8
    .kernarg_segment_size: 40
    .language:       OpenCL C
    .language_version:
      - 2
      - 0
    .max_flat_workgroup_size: 512
    .name:           _Z16postfinal_kernelPKfS0_S0_S0_Pf
    .private_segment_fixed_size: 0
    .sgpr_count:     30
    .sgpr_spill_count: 0
    .symbol:         _Z16postfinal_kernelPKfS0_S0_S0_Pf.kd
    .uniform_work_group_size: 1
    .uses_dynamic_stack: false
    .vgpr_count:     124
    .vgpr_spill_count: 0
    .wavefront_size: 64
  - .agpr_count:     16
    .args:
      - .offset:         0
        .size:           1136
        .value_kind:     by_value
    .group_segment_fixed_size: 34816
    .kernarg_segment_align: 8
    .kernarg_segment_size: 1136
    .language:       OpenCL C
    .language_version:
      - 2
      - 0
    .max_flat_workgroup_size: 256
    .name:           _Z14gemm_nt_kernelILi2EEv8GemmArgs
    .private_segment_fixed_size: 0
    .sgpr_count:     68
    .sgpr_spill_count: 0
    .symbol:         _Z14gemm_nt_kernelILi2EEv8GemmArgs.kd
    .uniform_work_group_size: 1
    .uses_dynamic_stack: false
    .vgpr_count:     140
    .vgpr_spill_count: 0
    .wavefront_size: 64
  - .agpr_count:     0
    .args:
      - .actual_access:  read_only
        .address_space:  global
        .offset:         0
        .size:           8
        .value_kind:     global_buffer
      - .offset:         8
        .size:           8
        .value_kind:     by_value
      - .actual_access:  read_only
        .address_space:  global
        .offset:         16
        .size:           8
        .value_kind:     global_buffer
      - .actual_access:  read_only
        .address_space:  global
        .offset:         24
        .size:           8
        .value_kind:     global_buffer
      - .actual_access:  read_only
        .address_space:  global
        .offset:         32
        .size:           8
        .value_kind:     global_buffer
      - .actual_access:  read_only
        .address_space:  global
        .offset:         40
        .size:           8
        .value_kind:     global_buffer
      - .actual_access:  write_only
        .address_space:  global
        .offset:         48
        .size:           8
        .value_kind:     global_buffer
      - .actual_access:  write_only
        .address_space:  global
        .offset:         56
        .size:           8
        .value_kind:     global_buffer
      - .offset:         64
        .size:           4
        .value_kind:     by_value
      - .offset:         72
        .size:           376
        .value_kind:     by_value
    .group_segment_fixed_size: 63488
    .kernarg_segment_align: 8
    .kernarg_segment_size: 448
    .language:       OpenCL C
    .language_version:
      - 2
      - 0
    .max_flat_workgroup_size: 512
    .name:           _Z15gru_mfma_kernelILi1EEvPKfmS1_S1_S1_S1_PfS2_i7PreArgs
    .private_segment_fixed_size: 0
    .sgpr_count:     36
    .sgpr_spill_count: 0
    .symbol:         _Z15gru_mfma_kernelILi1EEvPKfmS1_S1_S1_S1_PfS2_i7PreArgs.kd
    .uniform_work_group_size: 1
    .uses_dynamic_stack: false
    .vgpr_count:     232
    .vgpr_spill_count: 0
    .wavefront_size: 64
  - .agpr_count:     0
    .args:
      - .actual_access:  read_only
        .address_space:  global
        .offset:         0
        .size:           8
        .value_kind:     global_buffer
      - .offset:         8
        .size:           8
        .value_kind:     by_value
      - .actual_access:  read_only
        .address_space:  global
        .offset:         16
        .size:           8
        .value_kind:     global_buffer
      - .actual_access:  read_only
        .address_space:  global
        .offset:         24
        .size:           8
        .value_kind:     global_buffer
      - .actual_access:  read_only
        .address_space:  global
        .offset:         32
        .size:           8
        .value_kind:     global_buffer
      - .actual_access:  read_only
        .address_space:  global
        .offset:         40
        .size:           8
        .value_kind:     global_buffer
      - .actual_access:  write_only
        .address_space:  global
        .offset:         48
        .size:           8
        .value_kind:     global_buffer
      - .actual_access:  write_only
        .address_space:  global
        .offset:         56
        .size:           8
        .value_kind:     global_buffer
      - .offset:         64
        .size:           4
        .value_kind:     by_value
      - .offset:         72
        .size:           376
        .value_kind:     by_value
    .group_segment_fixed_size: 64480
    .kernarg_segment_align: 8
    .kernarg_segment_size: 448
    .language:       OpenCL C
    .language_version:
      - 2
      - 0
    .max_flat_workgroup_size: 512
    .name:           _Z15gru_mfma_kernelILi2EEvPKfmS1_S1_S1_S1_PfS2_i7PreArgs
    .private_segment_fixed_size: 0
    .sgpr_count:     50
    .sgpr_spill_count: 0
    .symbol:         _Z15gru_mfma_kernelILi2EEvPKfmS1_S1_S1_S1_PfS2_i7PreArgs.kd
    .uniform_work_group_size: 1
    .uses_dynamic_stack: false
    .vgpr_count:     232
    .vgpr_spill_count: 0
    .wavefront_size: 64
